# baseline (speedup 1.0000x reference)
_Z5k_aggPKDF16_PKhPKiS4_PKDv8_DF16_PKfPDF16_Pf:
	s_load_dwordx8 s[4:11], s[0:1], 0x8
	s_load_dwordx4 s[12:15], s[0:1], 0x28
	s_load_dwordx2 s[16:17], s[0:1], 0x38
	v_lshlrev_b32_e32 v2, 4, v0
	s_lshl_b32 s0, s2, 2
	s_lshl_b32 s1, s2, 3
	s_andn2_b32 s0, s0, 63
	s_and_b32 s1, s1, 56
	s_or_b32 s0, s0, s1
	s_lshr_b32 s1, s2, 1
	s_and_b32 s1, s1, 4
	s_or_b32 s0, s0, s1
	v_lshlrev_b32_e32 v1, 2, v0
	v_lshrrev_b32_e32 v52, 6, v0
	v_or_b32_e32 v3, s0, v52
	v_mov_b32_e32 v98, v2
	s_waitcnt lgkmcnt(0)
	v_readfirstlane_b32 s19, v52
	s_nop 3
	s_lshl_b32 s19, s19, 10
	s_mov_b32 m0, s19
	s_nop 0
	global_load_lds_dwordx4 v2, s[10:11]
	s_add_u32 m0, s19, 0x1000
	v_add_u32_e32 v96, 0x1000, v2
	global_load_lds_dwordx4 v96, s[10:11]
	s_add_u32 m0, s19, 0x2000
	v_add_u32_e32 v96, 0x2000, v2
	global_load_lds_dwordx4 v96, s[10:11]
	s_add_u32 m0, s19, 0x3000
	v_add_u32_e32 v96, 0x3000, v2
	global_load_lds_dwordx4 v96, s[10:11]
	s_add_u32 m0, s19, 0x4000
	v_add_u32_e32 v96, 0x4000, v2
	global_load_lds_dwordx4 v96, s[10:11]
	s_add_u32 m0, s19, 0x5000
	v_add_u32_e32 v96, 0x5000, v2
	global_load_lds_dwordx4 v96, s[10:11]
	s_add_u32 m0, s19, 0x6000
	v_add_u32_e32 v96, 0x6000, v2
	global_load_lds_dwordx4 v96, s[10:11]
	s_add_u32 m0, s19, 0x7000
	v_add_u32_e32 v96, 0x7000, v2
	global_load_lds_dwordx4 v96, s[10:11]
	v_mov_b32_e32 v97, 0
	ds_write2st64_b32 v1, v97, v97 offset0:128 offset1:132
	ds_write2st64_b32 v1, v97, v97 offset0:136 offset1:140
	s_movk_i32 s0, 0x186a
	v_cmp_gt_i32_e32 vcc, s0, v3
	s_and_saveexec_b64 s[0:1], vcc
	s_cbranch_execz .Lagg_invalid
	v_bfe_u32 v4, v0, 2, 4
	v_lshlrev_b32_e32 v53, 4, v3
	v_or_b32_e32 v10, v53, v4
	v_and_b32_e32 v54, 48, v2
	v_lshl_or_b32 v11, v10, 7, v54
	global_load_dwordx4 v[2:5], v11, s[4:5]
	global_load_dwordx4 v[6:9], v11, s[4:5] offset:64
	v_ashrrev_i32_e32 v11, 31, v10
	v_lshl_add_u64 v[10:11], v[10:11], 2, s[6:7]
	global_load_dwordx2 v[50:51], v[10:11], off
	s_waitcnt vmcnt(2)
	v_cvt_pk_f32_fp8_e32 v[88:89], v2
	v_cvt_pk_f32_fp8_sdwa v[90:91], v2 src0_sel:WORD_1
	v_cvt_pk_f32_fp8_e32 v[92:93], v3
	v_cvt_pk_f32_fp8_sdwa v[94:95], v3 src0_sel:WORD_1
	v_cvt_pk_f32_fp8_e32 v[76:77], v4
	v_cvt_pk_f32_fp8_sdwa v[80:81], v4 src0_sel:WORD_1
	v_cvt_pk_f32_fp8_e32 v[84:85], v5
	v_cvt_pk_f32_fp8_sdwa v[86:87], v5 src0_sel:WORD_1
	s_waitcnt vmcnt(1)
	v_cvt_pk_f32_fp8_e32 v[72:73], v6
	v_cvt_pk_f32_fp8_sdwa v[74:75], v6 src0_sel:WORD_1
	v_cvt_pk_f32_fp8_e32 v[78:79], v7
	v_cvt_pk_f32_fp8_sdwa v[82:83], v7 src0_sel:WORD_1
	v_cvt_pk_f32_fp8_e32 v[64:65], v8
	v_cvt_pk_f32_fp8_sdwa v[66:67], v8 src0_sel:WORD_1
	v_cvt_pk_f32_fp8_e32 v[68:69], v9
	v_cvt_pk_f32_fp8_sdwa v[70:71], v9 src0_sel:WORD_1
	s_waitcnt vmcnt(0)
	s_mov_b64 s[6:7], exec
	v_mov_b32_e32 v63, 0x186a0
	v_add_u32_e32 v106, 0, v50
	v_lshlrev_b32_e32 v106, 2, v106
	global_load_dwordx3 v[56:58], v106, s[8:9]
	v_add_u32_e32 v106, 3, v50
	v_lshlrev_b32_e32 v106, 2, v106
	global_load_dwordx3 v[60:62], v106, s[8:9]
	s_waitcnt vmcnt(0)
	v_add_u32_e32 v104, 0, v50
	v_cmp_lt_i32_e32 vcc, v104, v51
	s_nop 1
	v_cndmask_b32_e32 v105, v63, v56, vcc
	v_lshl_or_b32 v105, v105, 7, v54
	global_load_dwordx4 v[2:5], v105, s[4:5]
	global_load_dwordx4 v[6:9], v105, s[4:5] offset:64
	v_add_u32_e32 v104, 1, v50
	v_cmp_lt_i32_e32 vcc, v104, v51
	s_nop 1
	v_cndmask_b32_e32 v105, v63, v57, vcc
	v_lshl_or_b32 v105, v105, 7, v54
	global_load_dwordx4 v[10:13], v105, s[4:5]
	global_load_dwordx4 v[14:17], v105, s[4:5] offset:64
	v_add_u32_e32 v104, 2, v50
	v_cmp_lt_i32_e32 vcc, v104, v51
	s_nop 1
	v_cndmask_b32_e32 v105, v63, v58, vcc
	v_lshl_or_b32 v105, v105, 7, v54
	global_load_dwordx4 v[18:21], v105, s[4:5]
	global_load_dwordx4 v[22:25], v105, s[4:5] offset:64
	v_add_u32_e32 v106, 6, v50
	v_lshlrev_b32_e32 v106, 2, v106
	global_load_dwordx3 v[56:58], v106, s[8:9]
	v_add_u32_e32 v104, 3, v50
	v_cmp_lt_i32_e32 vcc, v104, v51
	s_nop 1
	v_cndmask_b32_e32 v105, v63, v60, vcc
	v_lshl_or_b32 v105, v105, 7, v54
	global_load_dwordx4 v[26:29], v105, s[4:5]
	global_load_dwordx4 v[30:33], v105, s[4:5] offset:64
	v_add_u32_e32 v104, 4, v50
	v_cmp_lt_i32_e32 vcc, v104, v51
	s_nop 1
	v_cndmask_b32_e32 v105, v63, v61, vcc
	v_lshl_or_b32 v105, v105, 7, v54
	global_load_dwordx4 v[34:37], v105, s[4:5]
	global_load_dwordx4 v[38:41], v105, s[4:5] offset:64
	v_add_u32_e32 v104, 5, v50
	v_cmp_lt_i32_e32 vcc, v104, v51
	s_nop 1
	v_cndmask_b32_e32 v105, v63, v62, vcc
	v_lshl_or_b32 v105, v105, 7, v54
	global_load_dwordx4 v[42:45], v105, s[4:5]
	global_load_dwordx4 v[46:49], v105, s[4:5] offset:64
	v_add_u32_e32 v106, 9, v50
	v_lshlrev_b32_e32 v106, 2, v106
	global_load_dwordx3 v[60:62], v106, s[8:9]
.Lagg_gloop:
	v_add_u32_e32 v104, 6, v50
	v_cmp_lt_i32_e32 vcc, v104, v51
	s_and_b64 vcc, exec, vcc
	s_cbranch_scc0 .Lagg_glast
	s_waitcnt vmcnt(7)
	v_add_u32_e32 v104, 6, v50
	v_cmp_lt_i32_e32 vcc, v104, v51
	v_cvt_pk_f32_fp8_e32 v[96:97], v2
	v_cvt_pk_f32_fp8_sdwa v[98:99], v2 src0_sel:WORD_1
	v_cvt_pk_f32_fp8_e32 v[100:101], v3
	v_cvt_pk_f32_fp8_sdwa v[102:103], v3 src0_sel:WORD_1
	v_pk_add_f32 v[88:89], v[88:89], v[96:97]
	v_pk_add_f32 v[90:91], v[90:91], v[98:99]
	v_pk_add_f32 v[92:93], v[92:93], v[100:101]
	v_pk_add_f32 v[94:95], v[94:95], v[102:103]
	v_cvt_pk_f32_fp8_e32 v[96:97], v4
	v_cvt_pk_f32_fp8_sdwa v[98:99], v4 src0_sel:WORD_1
	v_cvt_pk_f32_fp8_e32 v[100:101], v5
	v_cvt_pk_f32_fp8_sdwa v[102:103], v5 src0_sel:WORD_1
	v_pk_add_f32 v[76:77], v[76:77], v[96:97]
	v_pk_add_f32 v[80:81], v[80:81], v[98:99]
	v_pk_add_f32 v[84:85], v[84:85], v[100:101]
	v_pk_add_f32 v[86:87], v[86:87], v[102:103]
	v_cvt_pk_f32_fp8_e32 v[96:97], v6
	v_cvt_pk_f32_fp8_sdwa v[98:99], v6 src0_sel:WORD_1
	v_cvt_pk_f32_fp8_e32 v[100:101], v7
	v_cvt_pk_f32_fp8_sdwa v[102:103], v7 src0_sel:WORD_1
	v_pk_add_f32 v[72:73], v[72:73], v[96:97]
	v_pk_add_f32 v[74:75], v[74:75], v[98:99]
	v_pk_add_f32 v[78:79], v[78:79], v[100:101]
	v_pk_add_f32 v[82:83], v[82:83], v[102:103]
	v_cvt_pk_f32_fp8_e32 v[96:97], v8
	v_cvt_pk_f32_fp8_sdwa v[98:99], v8 src0_sel:WORD_1
	v_cvt_pk_f32_fp8_e32 v[100:101], v9
	v_cvt_pk_f32_fp8_sdwa v[102:103], v9 src0_sel:WORD_1
	v_pk_add_f32 v[64:65], v[64:65], v[96:97]
	v_pk_add_f32 v[66:67], v[66:67], v[98:99]
	v_pk_add_f32 v[68:69], v[68:69], v[100:101]
	v_pk_add_f32 v[70:71], v[70:71], v[102:103]
	v_cndmask_b32_e32 v105, v63, v56, vcc
	v_lshl_or_b32 v105, v105, 7, v54
	global_load_dwordx4 v[2:5], v105, s[4:5]
	global_load_dwordx4 v[6:9], v105, s[4:5] offset:64
	s_waitcnt vmcnt(9)
	v_add_u32_e32 v104, 7, v50
	v_cmp_lt_i32_e32 vcc, v104, v51
	v_cvt_pk_f32_fp8_e32 v[96:97], v10
	v_cvt_pk_f32_fp8_sdwa v[98:99], v10 src0_sel:WORD_1
	v_cvt_pk_f32_fp8_e32 v[100:101], v11
	v_cvt_pk_f32_fp8_sdwa v[102:103], v11 src0_sel:WORD_1
	v_pk_add_f32 v[88:89], v[88:89], v[96:97]
	v_pk_add_f32 v[90:91], v[90:91], v[98:99]
	v_pk_add_f32 v[92:93], v[92:93], v[100:101]
	v_pk_add_f32 v[94:95], v[94:95], v[102:103]
	v_cvt_pk_f32_fp8_e32 v[96:97], v12
	v_cvt_pk_f32_fp8_sdwa v[98:99], v12 src0_sel:WORD_1
	v_cvt_pk_f32_fp8_e32 v[100:101], v13
	v_cvt_pk_f32_fp8_sdwa v[102:103], v13 src0_sel:WORD_1
	v_pk_add_f32 v[76:77], v[76:77], v[96:97]
	v_pk_add_f32 v[80:81], v[80:81], v[98:99]
	v_pk_add_f32 v[84:85], v[84:85], v[100:101]
	v_pk_add_f32 v[86:87], v[86:87], v[102:103]
	v_cvt_pk_f32_fp8_e32 v[96:97], v14
	v_cvt_pk_f32_fp8_sdwa v[98:99], v14 src0_sel:WORD_1
	v_cvt_pk_f32_fp8_e32 v[100:101], v15
	v_cvt_pk_f32_fp8_sdwa v[102:103], v15 src0_sel:WORD_1
	v_pk_add_f32 v[72:73], v[72:73], v[96:97]
	v_pk_add_f32 v[74:75], v[74:75], v[98:99]
	v_pk_add_f32 v[78:79], v[78:79], v[100:101]
	v_pk_add_f32 v[82:83], v[82:83], v[102:103]
	v_cvt_pk_f32_fp8_e32 v[96:97], v16
	v_cvt_pk_f32_fp8_sdwa v[98:99], v16 src0_sel:WORD_1
	v_cvt_pk_f32_fp8_e32 v[100:101], v17
	v_cvt_pk_f32_fp8_sdwa v[102:103], v17 src0_sel:WORD_1
	v_pk_add_f32 v[64:65], v[64:65], v[96:97]
	v_pk_add_f32 v[66:67], v[66:67], v[98:99]
	v_pk_add_f32 v[68:69], v[68:69], v[100:101]
	v_pk_add_f32 v[70:71], v[70:71], v[102:103]
	v_cndmask_b32_e32 v105, v63, v57, vcc
	v_lshl_or_b32 v105, v105, 7, v54
	global_load_dwordx4 v[10:13], v105, s[4:5]
	global_load_dwordx4 v[14:17], v105, s[4:5] offset:64
	s_waitcnt vmcnt(11)
	v_add_u32_e32 v104, 8, v50
	v_cmp_lt_i32_e32 vcc, v104, v51
	v_cvt_pk_f32_fp8_e32 v[96:97], v18
	v_cvt_pk_f32_fp8_sdwa v[98:99], v18 src0_sel:WORD_1
	v_cvt_pk_f32_fp8_e32 v[100:101], v19
	v_cvt_pk_f32_fp8_sdwa v[102:103], v19 src0_sel:WORD_1
	v_pk_add_f32 v[88:89], v[88:89], v[96:97]
	v_pk_add_f32 v[90:91], v[90:91], v[98:99]
	v_pk_add_f32 v[92:93], v[92:93], v[100:101]
	v_pk_add_f32 v[94:95], v[94:95], v[102:103]
	v_cvt_pk_f32_fp8_e32 v[96:97], v20
	v_cvt_pk_f32_fp8_sdwa v[98:99], v20 src0_sel:WORD_1
	v_cvt_pk_f32_fp8_e32 v[100:101], v21
	v_cvt_pk_f32_fp8_sdwa v[102:103], v21 src0_sel:WORD_1
	v_pk_add_f32 v[76:77], v[76:77], v[96:97]
	v_pk_add_f32 v[80:81], v[80:81], v[98:99]
	v_pk_add_f32 v[84:85], v[84:85], v[100:101]
	v_pk_add_f32 v[86:87], v[86:87], v[102:103]
	v_cvt_pk_f32_fp8_e32 v[96:97], v22
	v_cvt_pk_f32_fp8_sdwa v[98:99], v22 src0_sel:WORD_1
	v_cvt_pk_f32_fp8_e32 v[100:101], v23
	v_cvt_pk_f32_fp8_sdwa v[102:103], v23 src0_sel:WORD_1
	v_pk_add_f32 v[72:73], v[72:73], v[96:97]
	v_pk_add_f32 v[74:75], v[74:75], v[98:99]
	v_pk_add_f32 v[78:79], v[78:79], v[100:101]
	v_pk_add_f32 v[82:83], v[82:83], v[102:103]
	v_cvt_pk_f32_fp8_e32 v[96:97], v24
	v_cvt_pk_f32_fp8_sdwa v[98:99], v24 src0_sel:WORD_1
	v_cvt_pk_f32_fp8_e32 v[100:101], v25
	v_cvt_pk_f32_fp8_sdwa v[102:103], v25 src0_sel:WORD_1
	v_pk_add_f32 v[64:65], v[64:65], v[96:97]
	v_pk_add_f32 v[66:67], v[66:67], v[98:99]
	v_pk_add_f32 v[68:69], v[68:69], v[100:101]
	v_pk_add_f32 v[70:71], v[70:71], v[102:103]
	v_cndmask_b32_e32 v105, v63, v58, vcc
	v_lshl_or_b32 v105, v105, 7, v54
	global_load_dwordx4 v[18:21], v105, s[4:5]
	global_load_dwordx4 v[22:25], v105, s[4:5] offset:64
	v_add_u32_e32 v106, 12, v50
	v_lshlrev_b32_e32 v106, 2, v106
	global_load_dwordx3 v[56:58], v106, s[8:9]
	s_waitcnt vmcnt(7)
	v_add_u32_e32 v104, 9, v50
	v_cmp_lt_i32_e32 vcc, v104, v51
	v_cvt_pk_f32_fp8_e32 v[96:97], v26
	v_cvt_pk_f32_fp8_sdwa v[98:99], v26 src0_sel:WORD_1
	v_cvt_pk_f32_fp8_e32 v[100:101], v27
	v_cvt_pk_f32_fp8_sdwa v[102:103], v27 src0_sel:WORD_1
	v_pk_add_f32 v[88:89], v[88:89], v[96:97]
	v_pk_add_f32 v[90:91], v[90:91], v[98:99]
	v_pk_add_f32 v[92:93], v[92:93], v[100:101]
	v_pk_add_f32 v[94:95], v[94:95], v[102:103]
	v_cvt_pk_f32_fp8_e32 v[96:97], v28
	v_cvt_pk_f32_fp8_sdwa v[98:99], v28 src0_sel:WORD_1
	v_cvt_pk_f32_fp8_e32 v[100:101], v29
	v_cvt_pk_f32_fp8_sdwa v[102:103], v29 src0_sel:WORD_1
	v_pk_add_f32 v[76:77], v[76:77], v[96:97]
	v_pk_add_f32 v[80:81], v[80:81], v[98:99]
	v_pk_add_f32 v[84:85], v[84:85], v[100:101]
	v_pk_add_f32 v[86:87], v[86:87], v[102:103]
	v_cvt_pk_f32_fp8_e32 v[96:97], v30
	v_cvt_pk_f32_fp8_sdwa v[98:99], v30 src0_sel:WORD_1
	v_cvt_pk_f32_fp8_e32 v[100:101], v31
	v_cvt_pk_f32_fp8_sdwa v[102:103], v31 src0_sel:WORD_1
	v_pk_add_f32 v[72:73], v[72:73], v[96:97]
	v_pk_add_f32 v[74:75], v[74:75], v[98:99]
	v_pk_add_f32 v[78:79], v[78:79], v[100:101]
	v_pk_add_f32 v[82:83], v[82:83], v[102:103]
	v_cvt_pk_f32_fp8_e32 v[96:97], v32
	v_cvt_pk_f32_fp8_sdwa v[98:99], v32 src0_sel:WORD_1
	v_cvt_pk_f32_fp8_e32 v[100:101], v33
	v_cvt_pk_f32_fp8_sdwa v[102:103], v33 src0_sel:WORD_1
	v_pk_add_f32 v[64:65], v[64:65], v[96:97]
	v_pk_add_f32 v[66:67], v[66:67], v[98:99]
	v_pk_add_f32 v[68:69], v[68:69], v[100:101]
	v_pk_add_f32 v[70:71], v[70:71], v[102:103]
	v_cndmask_b32_e32 v105, v63, v60, vcc
	v_lshl_or_b32 v105, v105, 7, v54
	global_load_dwordx4 v[26:29], v105, s[4:5]
	global_load_dwordx4 v[30:33], v105, s[4:5] offset:64
	s_waitcnt vmcnt(9)
	v_add_u32_e32 v104, 10, v50
	v_cmp_lt_i32_e32 vcc, v104, v51
	v_cvt_pk_f32_fp8_e32 v[96:97], v34
	v_cvt_pk_f32_fp8_sdwa v[98:99], v34 src0_sel:WORD_1
	v_cvt_pk_f32_fp8_e32 v[100:101], v35
	v_cvt_pk_f32_fp8_sdwa v[102:103], v35 src0_sel:WORD_1
	v_pk_add_f32 v[88:89], v[88:89], v[96:97]
	v_pk_add_f32 v[90:91], v[90:91], v[98:99]
	v_pk_add_f32 v[92:93], v[92:93], v[100:101]
	v_pk_add_f32 v[94:95], v[94:95], v[102:103]
	v_cvt_pk_f32_fp8_e32 v[96:97], v36
	v_cvt_pk_f32_fp8_sdwa v[98:99], v36 src0_sel:WORD_1
	v_cvt_pk_f32_fp8_e32 v[100:101], v37
	v_cvt_pk_f32_fp8_sdwa v[102:103], v37 src0_sel:WORD_1
	v_pk_add_f32 v[76:77], v[76:77], v[96:97]
	v_pk_add_f32 v[80:81], v[80:81], v[98:99]
	v_pk_add_f32 v[84:85], v[84:85], v[100:101]
	v_pk_add_f32 v[86:87], v[86:87], v[102:103]
	v_cvt_pk_f32_fp8_e32 v[96:97], v38
	v_cvt_pk_f32_fp8_sdwa v[98:99], v38 src0_sel:WORD_1
	v_cvt_pk_f32_fp8_e32 v[100:101], v39
	v_cvt_pk_f32_fp8_sdwa v[102:103], v39 src0_sel:WORD_1
	v_pk_add_f32 v[72:73], v[72:73], v[96:97]
	v_pk_add_f32 v[74:75], v[74:75], v[98:99]
	v_pk_add_f32 v[78:79], v[78:79], v[100:101]
	v_pk_add_f32 v[82:83], v[82:83], v[102:103]
	v_cvt_pk_f32_fp8_e32 v[96:97], v40
	v_cvt_pk_f32_fp8_sdwa v[98:99], v40 src0_sel:WORD_1
	v_cvt_pk_f32_fp8_e32 v[100:101], v41
	v_cvt_pk_f32_fp8_sdwa v[102:103], v41 src0_sel:WORD_1
	v_pk_add_f32 v[64:65], v[64:65], v[96:97]
	v_pk_add_f32 v[66:67], v[66:67], v[98:99]
	v_pk_add_f32 v[68:69], v[68:69], v[100:101]
	v_pk_add_f32 v[70:71], v[70:71], v[102:103]
	v_cndmask_b32_e32 v105, v63, v61, vcc
	v_lshl_or_b32 v105, v105, 7, v54
	global_load_dwordx4 v[34:37], v105, s[4:5]
	global_load_dwordx4 v[38:41], v105, s[4:5] offset:64
	s_waitcnt vmcnt(11)
	v_add_u32_e32 v104, 11, v50
	v_cmp_lt_i32_e32 vcc, v104, v51
	v_cvt_pk_f32_fp8_e32 v[96:97], v42
	v_cvt_pk_f32_fp8_sdwa v[98:99], v42 src0_sel:WORD_1
	v_cvt_pk_f32_fp8_e32 v[100:101], v43
	v_cvt_pk_f32_fp8_sdwa v[102:103], v43 src0_sel:WORD_1
	v_pk_add_f32 v[88:89], v[88:89], v[96:97]
	v_pk_add_f32 v[90:91], v[90:91], v[98:99]
	v_pk_add_f32 v[92:93], v[92:93], v[100:101]
	v_pk_add_f32 v[94:95], v[94:95], v[102:103]
	v_cvt_pk_f32_fp8_e32 v[96:97], v44
	v_cvt_pk_f32_fp8_sdwa v[98:99], v44 src0_sel:WORD_1
	v_cvt_pk_f32_fp8_e32 v[100:101], v45
	v_cvt_pk_f32_fp8_sdwa v[102:103], v45 src0_sel:WORD_1
	v_pk_add_f32 v[76:77], v[76:77], v[96:97]
	v_pk_add_f32 v[80:81], v[80:81], v[98:99]
	v_pk_add_f32 v[84:85], v[84:85], v[100:101]
	v_pk_add_f32 v[86:87], v[86:87], v[102:103]
	v_cvt_pk_f32_fp8_e32 v[96:97], v46
	v_cvt_pk_f32_fp8_sdwa v[98:99], v46 src0_sel:WORD_1
	v_cvt_pk_f32_fp8_e32 v[100:101], v47
	v_cvt_pk_f32_fp8_sdwa v[102:103], v47 src0_sel:WORD_1
	v_pk_add_f32 v[72:73], v[72:73], v[96:97]
	v_pk_add_f32 v[74:75], v[74:75], v[98:99]
	v_pk_add_f32 v[78:79], v[78:79], v[100:101]
	v_pk_add_f32 v[82:83], v[82:83], v[102:103]
	v_cvt_pk_f32_fp8_e32 v[96:97], v48
	v_cvt_pk_f32_fp8_sdwa v[98:99], v48 src0_sel:WORD_1
	v_cvt_pk_f32_fp8_e32 v[100:101], v49
	v_cvt_pk_f32_fp8_sdwa v[102:103], v49 src0_sel:WORD_1
	v_pk_add_f32 v[64:65], v[64:65], v[96:97]
	v_pk_add_f32 v[66:67], v[66:67], v[98:99]
	v_pk_add_f32 v[68:69], v[68:69], v[100:101]
	v_pk_add_f32 v[70:71], v[70:71], v[102:103]
	v_cndmask_b32_e32 v105, v63, v62, vcc
	v_lshl_or_b32 v105, v105, 7, v54
	global_load_dwordx4 v[42:45], v105, s[4:5]
	global_load_dwordx4 v[46:49], v105, s[4:5] offset:64
	v_add_u32_e32 v106, 15, v50
	v_lshlrev_b32_e32 v106, 2, v106
	global_load_dwordx3 v[60:62], v106, s[8:9]
	v_add_u32_e32 v50, 6, v50
	s_branch .Lagg_gloop
